# P2 GLA prep: gate activation load waited only after the gate-weight loads are issued (one exposed round trip per unit)
# speedup vs baseline: 1.0884x; 1.0056x over previous
; __device__ __forceinline__ void gla_prep_unit(Frame& F, int unit) {
;     ...
;     const int d = tid & 127, cg = tid >> 7;
;     bf16_t qv[16], kv[16];
; #pragma unroll
;     for (int i = 0; i < 16; ++i) { const bf16_t* pr = PROJ + (m0 + cg * 16 + i) * LDP + h * 128 + d; qv[i] = pr[C_GQ]; kv[i] = pr[C_GK]; }
;     { const int c = tid >> 3, r2 = (tid & 7) * 2; const unsigned w = *(const unsigned*)(PROJ + (m0 + c) * LDP + C_GA + r2); gaS[c * 16 + r2] = bflo(w); gaS[c * 16 + r2 + 1] = bfhi(w); }
;     float w2r[16];
; #pragma unroll
;     for (int r = 0; r < 16; ++r) w2r[r] = F.w2[r * 1024 + h * 128 + d];
;     const float bias = F.gb[h * 128 + d];
.LBB0_264:
	s_ashr_i32 s58, s57, 10
	s_ashr_i32 s59, s58, 31
	s_and_b32 s0, s57, 0x380
	s_lshl_b64 s[58:59], s[58:59], 13
	s_and_b32 s1, s3, 0x1fc0
	s_or_b32 s1, s58, s1
	s_lshl_b32 s28, s0, 1
	v_or_b32_e32 v4, s1, v12
	v_lshl_add_u64 v[2:3], v[14:15], 0, s[28:29]
	v_mad_u64_u32 v[2:3], s[60:61], v4, s43, v[2:3]
	v_or_b32_e32 v6, s1, v168
	v_mov_b64_e32 v[4:5], s[96:97]
	v_mad_u64_u32 v[4:5], s[60:61], v6, s43, v[4:5]
	v_mad_i32_i24 v5, s59, v87, v5
	v_lshl_add_u64 v[4:5], v[4:5], 0, v[8:9]
	v_add_co_u32_e32 v4, vcc, s44, v4
	v_mad_i32_i24 v3, s59, v87, v3
	s_nop 0
	v_addc_co_u32_e32 v5, vcc, 0, v5, vcc
	global_load_dword v193, v[4:5], off offset:1024
	v_add_co_u32_e32 v6, vcc, s44, v2
	s_mov_b32 s1, 0xd000
	s_nop 0
	v_addc_co_u32_e32 v7, vcc, 0, v3, vcc
	v_add_co_u32_e32 v58, vcc, s46, v2
	global_load_ushort v119, v[6:7], off offset:1536
	s_nop 0
	v_addc_co_u32_e32 v59, vcc, 0, v3, vcc
	global_load_ushort v117, v[58:59], off offset:3072
	v_add_co_u32_e32 v58, vcc, s1, v2
	s_mov_b32 s1, 0x9000
	s_nop 0
	v_addc_co_u32_e32 v59, vcc, 0, v3, vcc
	v_add_co_u32_e32 v60, vcc, s1, v2
	s_mov_b32 s1, 0x11000
	s_nop 0
	v_addc_co_u32_e32 v61, vcc, 0, v3, vcc
	global_load_ushort v118, v[58:59], off offset:512
	global_load_ushort v120, v[2:3], off
	global_load_ushort v114, v[60:61], off offset:1024
	global_load_ushort v115, v[2:3], off offset:2048
	global_load_ushort v111, v[6:7], off offset:3584
	global_load_ushort v112, v[58:59], off offset:2560
	v_add_co_u32_e32 v6, vcc, s1, v2
	s_mov_b32 s1, 0x15000
	s_nop 0
	v_addc_co_u32_e32 v7, vcc, 0, v3, vcc
	global_load_ushort v110, v[6:7], off offset:2048
	v_add_co_u32_e32 v6, vcc, s1, v2
	s_mov_b32 s1, 0x1a000
	s_nop 0
	v_addc_co_u32_e32 v7, vcc, 0, v3, vcc
	global_load_ushort v109, v[6:7], off offset:3584
	v_add_co_u32_e32 v6, vcc, s1, v2
	s_mov_b32 s1, 0x1e000
	s_nop 0
	v_addc_co_u32_e32 v7, vcc, 0, v3, vcc
	v_add_co_u32_e32 v58, vcc, s1, v2
	s_mov_b32 s1, 0x12000
	s_nop 0
	v_addc_co_u32_e32 v59, vcc, 0, v3, vcc
	global_load_ushort v107, v[6:7], off offset:1024
	global_load_ushort v104, v[58:59], off offset:2560
	v_add_co_u32_e32 v58, vcc, s1, v2
	s_mov_b32 s1, 0x16000
	s_nop 0
	v_addc_co_u32_e32 v59, vcc, 0, v3, vcc
	global_load_ushort v100, v[58:59], off
	global_load_ushort v101, v[6:7], off offset:3072
	v_add_co_u32_e32 v6, vcc, s1, v2
	s_mov_b32 s1, 0x1f000
	s_nop 0
	v_addc_co_u32_e32 v7, vcc, 0, v3, vcc
	global_load_ushort v102, v[6:7], off offset:1536
	v_add_co_u32_e32 v6, vcc, s1, v2
	s_mov_b32 s1, 0x23000
	s_nop 0
	v_addc_co_u32_e32 v7, vcc, 0, v3, vcc
	global_load_ushort v105, v[6:7], off offset:512
	v_add_co_u32_e32 v6, vcc, s1, v2
	s_mov_b32 s1, 0x27000
	s_nop 0
	v_addc_co_u32_e32 v7, vcc, 0, v3, vcc
	v_add_co_u32_e32 v58, vcc, s1, v2
	s_mov_b32 s1, 0x2b000
	s_nop 0
	v_addc_co_u32_e32 v59, vcc, 0, v3, vcc
	v_add_co_u32_e32 v60, vcc, s1, v2
	s_mov_b32 s1, 0x30000
	s_nop 0
	v_addc_co_u32_e32 v61, vcc, 0, v3, vcc
	global_load_ushort v116, v[6:7], off
	global_load_ushort v113, v[58:59], off offset:1536
	global_load_ushort v108, v[60:61], off offset:3072
	v_add_co_u32_e32 v60, vcc, s1, v2
	s_mov_b32 s1, 0x2c000
	s_nop 0
	v_addc_co_u32_e32 v61, vcc, 0, v3, vcc
	global_load_ushort v106, v[60:61], off offset:512
	global_load_ushort v99, v[6:7], off offset:2048
	v_add_co_u32_e32 v6, vcc, s1, v2
	s_mov_b32 s1, 0x34000
	s_nop 0
	v_addc_co_u32_e32 v7, vcc, 0, v3, vcc
	global_load_ushort v103, v[6:7], off offset:1024
	global_load_ushort v97, v[58:59], off offset:3584
	global_load_ushort v98, v[60:61], off offset:2560
	v_add_co_u32_e32 v6, vcc, s1, v2
	s_mov_b32 s1, 0x38000
	s_nop 0
	v_addc_co_u32_e32 v7, vcc, 0, v3, vcc
	global_load_ushort v96, v[6:7], off offset:2048
	v_add_co_u32_e32 v6, vcc, s1, v2
	s_mov_b32 s1, 0x3d000
	s_nop 0
	v_addc_co_u32_e32 v7, vcc, 0, v3, vcc
	global_load_ushort v95, v[6:7], off offset:3584
	v_add_co_u32_e32 v6, vcc, s1, v2
	s_mov_b32 s1, 0x41000
	s_nop 0
	v_addc_co_u32_e32 v7, vcc, 0, v3, vcc
	v_add_co_u32_e32 v58, vcc, s1, v2
	s_mov_b32 s1, 0x35000
	s_nop 0
	v_addc_co_u32_e32 v59, vcc, 0, v3, vcc
	global_load_ushort v94, v[6:7], off offset:1024
	global_load_ushort v93, v[58:59], off offset:2560
	v_add_co_u32_e32 v58, vcc, s1, v2
	s_mov_b32 s1, 0x39000
	s_nop 0
	v_addc_co_u32_e32 v59, vcc, 0, v3, vcc
	global_load_ushort v91, v[58:59], off
	global_load_ushort v92, v[6:7], off offset:3072
	v_add_co_u32_e32 v6, vcc, s1, v2
	s_mov_b32 s1, 0x42000
	s_nop 0
	v_addc_co_u32_e32 v7, vcc, 0, v3, vcc
	v_add_co_u32_e32 v2, vcc, s1, v2
	v_readlane_b32 s68, v254, 36
	s_nop 0
	v_addc_co_u32_e32 v3, vcc, 0, v3, vcc
	global_load_ushort v89, v[6:7], off offset:1536
	global_load_ushort v90, v[2:3], off offset:512
	v_or_b32_e32 v2, s0, v10
	v_readlane_b32 s69, v254, 37
	v_readlane_b32 s70, v254, 38
	v_readlane_b32 s71, v254, 39
	v_readlane_b32 s72, v254, 40
	v_readlane_b32 s73, v254, 41
	v_readlane_b32 s74, v254, 42
	v_readlane_b32 s75, v254, 43
	v_readlane_b32 s76, v254, 44
	v_readlane_b32 s77, v254, 45
	v_lshlrev_b32_e32 v122, 2, v2
	v_mov_b32_e32 v123, v9
	v_readlane_b32 s78, v254, 46
	v_readlane_b32 s79, v254, 47
	v_readlane_b32 s80, v254, 48
	v_readlane_b32 s81, v254, 49
	v_readlane_b32 s82, v254, 50
	v_readlane_b32 s83, v254, 51
	s_mov_b64 s[68:69], s[76:77]
	v_lshl_add_u64 v[124:125], s[68:69], 0, v[122:123]
	s_movk_i32 s0, 0x2000
	v_add_co_u32_e32 v4, vcc, s0, v124
	s_movk_i32 s0, 0x6000
	s_nop 0
	v_addc_co_u32_e32 v5, vcc, 0, v125, vcc
	v_add_co_u32_e32 v60, vcc, s44, v124
	global_load_dword v2, v122, s[68:69]
	s_nop 0
	v_addc_co_u32_e32 v61, vcc, 0, v125, vcc
	global_load_dword v6, v[4:5], off offset:-4096
	s_nop 0
	global_load_dword v4, v[4:5], off
	s_nop 0
	global_load_dword v58, v[60:61], off offset:-4096
	global_load_dword v3, v[60:61], off
	v_add_co_u32_e32 v60, vcc, s0, v124
	s_mov_b32 s0, 0xa000
	s_nop 0
	v_addc_co_u32_e32 v61, vcc, 0, v125, vcc
	global_load_dword v7, v[60:61], off offset:-4096
	global_load_dword v5, v[60:61], off
	v_add_co_u32_e32 v60, vcc, s46, v124
	s_mov_b64 s[70:71], s[78:79]
	s_nop 0
	v_addc_co_u32_e32 v61, vcc, 0, v125, vcc
	v_add_co_u32_e32 v62, vcc, s0, v124
	global_load_dword v59, v[60:61], off offset:-4096
	s_nop 0
	global_load_dword v60, v[60:61], off
	v_addc_co_u32_e32 v63, vcc, 0, v125, vcc
	v_add_co_u32_e32 v126, vcc, s47, v124
	global_load_dword v64, v[62:63], off offset:-4096
	s_nop 0
	global_load_dword v62, v[62:63], off
	v_addc_co_u32_e32 v127, vcc, 0, v125, vcc
	global_load_dword v66, v[126:127], off offset:-4096
	global_load_dword v61, v[126:127], off
	v_add_co_u32_e32 v126, vcc, s48, v124
	s_mov_b64 s[72:73], s[80:81]
	s_nop 0
	v_addc_co_u32_e32 v127, vcc, 0, v125, vcc
	v_add_co_u32_e32 v124, vcc, s49, v124
	global_load_dword v65, v[126:127], off offset:-4096
	global_load_dword v63, v[126:127], off
	v_addc_co_u32_e32 v125, vcc, 0, v125, vcc
	global_load_dword v67, v[124:125], off
	global_load_dword v121, v122, s[70:71]
	s_waitcnt vmcnt(49)
	v_lshlrev_b32_e32 v194, 16, v193
	v_and_b32_e32 v195, 0xffff0000, v193
	ds_write_b64 v11, v[194:195]
	s_waitcnt lgkmcnt(0)
	s_barrier
; #define LAS __attribute__((address_space(3)))
; __device__ __forceinline__ void gla_prep_unit(Frame& F, int unit) {
;     ...
;     float bl[16]; float run = 0.f;
; #pragma unroll
;     for (int i = 0; i < 16; ++i) { const int c = cg * 16 + i; float z = bias;
; #pragma unroll
;         for (int r4 = 0; r4 < 4; ++r4) { const f32x4 g4 = *(const LAS f32x4*)(gaS + c * 16 + 4 * r4); z += g4.x * w2r[4 * r4] + g4.y * w2r[4 * r4 + 1] + g4.z * w2r[4 * r4 + 2] + g4.w * w2r[4 * r4 + 3]; }
;         const float ls = fminf(z, 0.f) - __logf(1.0f + __expf(-fabsf(z)));
;         run += ls * (1.f / 16.f); bl[i] = run; }
	ds_read_b128 v[122:125], v13
	ds_read_b128 v[126:129], v13 offset:16
	ds_read_b128 v[132:135], v13 offset:32
	ds_read_b128 v[136:139], v13 offset:48
	s_mov_b64 s[74:75], s[82:83]
	s_waitcnt lgkmcnt(3)
	v_mov_b32_e32 v140, v122
	s_waitcnt lgkmcnt(2)
	v_mov_b32_e32 v141, v126
	v_mov_b32_e32 v126, v123
	s_waitcnt vmcnt(11)
	v_pk_mul_f32 v[122:123], v[6:7], v[126:127]
	s_nop 0
	v_pk_fma_f32 v[122:123], v[2:3], v[140:141], v[122:123]
	v_mov_b32_e32 v126, v124
	v_mov_b32_e32 v127, v128
	s_waitcnt vmcnt(10)
	v_pk_fma_f32 v[122:123], v[4:5], v[126:127], v[122:123]
	v_mov_b32_e32 v128, v125
	s_waitcnt vmcnt(9)
	v_pk_fma_f32 v[122:123], v[58:59], v[128:129], v[122:123]
	s_waitcnt vmcnt(0)
	v_add_f32_e32 v122, v121, v122
	v_add_f32_e32 v126, v122, v123
	s_waitcnt lgkmcnt(0)
	v_mov_b32_e32 v123, v136
	v_mov_b32_e32 v136, v133
	v_mov_b32_e32 v122, v132
	v_pk_mul_f32 v[124:125], v[64:65], v[136:137]
	s_nop 0
	v_pk_fma_f32 v[122:123], v[60:61], v[122:123], v[124:125]
	v_mov_b32_e32 v124, v134
	v_mov_b32_e32 v125, v138
	v_pk_fma_f32 v[122:123], v[62:63], v[124:125], v[122:123]
	v_mov_b32_e32 v138, v135
	v_pk_fma_f32 v[122:123], v[66:67], v[138:139], v[122:123]
	s_nop 0
	v_add_f32_e32 v122, v126, v122
	v_add_f32_e32 v122, v122, v123
	v_min_f32_e32 v123, 0, v122
	v_mul_f32_e64 v122, |v122|, s50
	v_exp_f32_e32 v122, v122
	s_nop 0
	v_add_f32_e32 v122, 1.0, v122
	v_cmp_gt_f32_e32 vcc, s51, v122
	s_nop 1
	v_cndmask_b32_e64 v124, 0, 32, vcc
	v_ldexp_f32 v122, v122, v124
	v_log_f32_e32 v122, v122
	s_nop 0
	v_mul_f32_e32 v124, 0x3f317217, v122
	v_fma_f32 v124, v122, s52, -v124
	v_fmac_f32_e32 v124, 0x3377d1cf, v122
	v_fmac_f32_e32 v124, 0x3f317217, v122
	v_cmp_lt_f32_e64 s[0:1], |v122|, s53
	s_nop 1
	v_cndmask_b32_e64 v122, v122, v124, s[0:1]
	v_cndmask_b32_e32 v124, 0, v88, vcc
	v_sub_f32_e32 v122, v122, v124
	ds_read_b128 v[124:127], v13 offset:64
	ds_read_b128 v[132:135], v13 offset:80
	v_sub_f32_e32 v122, v123, v122
	v_fma_f32 v122, v122, s54, 0
	s_waitcnt lgkmcnt(1)
	v_mov_b32_e32 v128, v124
	s_waitcnt lgkmcnt(0)
	v_mov_b32_e32 v129, v132
	v_mov_b32_e32 v132, v125
	v_pk_mul_f32 v[124:125], v[6:7], v[132:133]
	s_nop 0
	v_pk_fma_f32 v[124:125], v[2:3], v[128:129], v[124:125]
	v_mov_b32_e32 v128, v126
	v_mov_b32_e32 v129, v134
	v_pk_fma_f32 v[124:125], v[4:5], v[128:129], v[124:125]
	v_mov_b32_e32 v134, v127
	v_pk_fma_f32 v[124:125], v[58:59], v[134:135], v[124:125]
	s_nop 0
	v_add_f32_e32 v123, v121, v124
	v_add_f32_e32 v123, v123, v125
	ds_read_b128 v[124:127], v13 offset:96
	ds_read_b128 v[132:135], v13 offset:112
	s_waitcnt lgkmcnt(1)
	v_mov_b32_e32 v128, v124
	s_waitcnt lgkmcnt(0)
	v_mov_b32_e32 v129, v132
	v_mov_b32_e32 v132, v125
	v_pk_mul_f32 v[124:125], v[64:65], v[132:133]
	s_nop 0
	v_pk_fma_f32 v[124:125], v[60:61], v[128:129], v[124:125]
	v_mov_b32_e32 v128, v126
	v_mov_b32_e32 v129, v134
	v_pk_fma_f32 v[124:125], v[62:63], v[128:129], v[124:125]
	v_mov_b32_e32 v134, v127
	v_pk_fma_f32 v[124:125], v[66:67], v[134:135], v[124:125]
	s_nop 0
	v_add_f32_e32 v123, v123, v124
	v_add_f32_e32 v123, v123, v125
	v_min_f32_e32 v124, 0, v123
	v_mul_f32_e64 v123, |v123|, s50
	v_exp_f32_e32 v123, v123
	s_nop 0
	v_add_f32_e32 v123, 1.0, v123
	v_cmp_gt_f32_e32 vcc, s51, v123
	s_nop 1
	v_cndmask_b32_e64 v125, 0, 32, vcc
	v_ldexp_f32 v123, v123, v125
	v_log_f32_e32 v123, v123
	s_nop 0
	v_mul_f32_e32 v125, 0x3f317217, v123
	v_fma_f32 v125, v123, s52, -v125
	v_fmac_f32_e32 v125, 0x3377d1cf, v123
	v_fmac_f32_e32 v125, 0x3f317217, v123
	v_cmp_lt_f32_e64 s[0:1], |v123|, s53
	s_nop 1
	v_cndmask_b32_e64 v123, v123, v125, s[0:1]
	v_cndmask_b32_e32 v125, 0, v88, vcc
	v_sub_f32_e32 v123, v123, v125
	v_sub_f32_e32 v123, v124, v123
	ds_read_b128 v[124:127], v13 offset:128
	ds_read_b128 v[132:135], v13 offset:144
	v_fmamk_f32 v123, v123, 0x3d800000, v122
	s_waitcnt lgkmcnt(1)
	v_mov_b32_e32 v128, v124
	s_waitcnt lgkmcnt(0)
	v_mov_b32_e32 v129, v132
	v_mov_b32_e32 v132, v125
	v_pk_mul_f32 v[124:125], v[6:7], v[132:133]
	s_nop 0
	v_pk_fma_f32 v[124:125], v[2:3], v[128:129], v[124:125]
	v_mov_b32_e32 v128, v126
	v_mov_b32_e32 v129, v134
	v_pk_fma_f32 v[124:125], v[4:5], v[128:129], v[124:125]
	v_mov_b32_e32 v134, v127
	v_pk_fma_f32 v[124:125], v[58:59], v[134:135], v[124:125]
	s_nop 0
	v_add_f32_e32 v124, v121, v124
	v_add_f32_e32 v136, v124, v125
	ds_read_b128 v[124:127], v13 offset:160
	ds_read_b128 v[132:135], v13 offset:176
	s_waitcnt lgkmcnt(1)
	v_mov_b32_e32 v128, v124
	s_waitcnt lgkmcnt(0)
	v_mov_b32_e32 v129, v132
	v_mov_b32_e32 v132, v125
	v_pk_mul_f32 v[124:125], v[64:65], v[132:133]
	s_nop 0
	v_pk_fma_f32 v[124:125], v[60:61], v[128:129], v[124:125]
	v_mov_b32_e32 v128, v126
	v_mov_b32_e32 v129, v134
	v_pk_fma_f32 v[124:125], v[62:63], v[128:129], v[124:125]
	v_mov_b32_e32 v134, v127
	v_pk_fma_f32 v[124:125], v[66:67], v[134:135], v[124:125]
	s_nop 0
	v_add_f32_e32 v124, v136, v124
	v_add_f32_e32 v124, v124, v125
	v_min_f32_e32 v125, 0, v124
	v_mul_f32_e64 v124, |v124|, s50
	v_exp_f32_e32 v124, v124
	s_nop 0
	v_add_f32_e32 v124, 1.0, v124
	v_cmp_gt_f32_e32 vcc, s51, v124
	s_nop 1
	v_cndmask_b32_e64 v126, 0, 32, vcc
	v_ldexp_f32 v124, v124, v126
	v_log_f32_e32 v124, v124
	s_nop 0
	v_mul_f32_e32 v126, 0x3f317217, v124
	v_fma_f32 v126, v124, s52, -v126
	v_fmac_f32_e32 v126, 0x3377d1cf, v124
	v_fmac_f32_e32 v126, 0x3f317217, v124
	v_cmp_lt_f32_e64 s[0:1], |v124|, s53
	s_nop 1
	v_cndmask_b32_e64 v124, v124, v126, s[0:1]
	v_cndmask_b32_e32 v126, 0, v88, vcc
	v_sub_f32_e32 v124, v124, v126
	ds_read_b128 v[126:129], v13 offset:192
	ds_read_b128 v[132:135], v13 offset:208
	v_sub_f32_e32 v124, v125, v124
	v_fmamk_f32 v124, v124, 0x3d800000, v123
	s_waitcnt lgkmcnt(1)
; #define LAS __attribute__((address_space(3)))
; __device__ __forceinline__ void gla_prep_unit(Frame& F, int unit) {
;     ...
;     for (int i = 0; i < 16; ++i) { const int c = cg * 16 + i; float z = bias;
; #pragma unroll
;         for (int r4 = 0; r4 < 4; ++r4) { const f32x4 g4 = *(const LAS f32x4*)(gaS + c * 16 + 4 * r4); z += g4.x * w2r[4 * r4] + g4.y * w2r[4 * r4 + 1] + g4.z * w2r[4 * r4 + 2] + g4.w * w2r[4 * r4 + 3]; }
;         const float ls = fminf(z, 0.f) - __logf(1.0f + __expf(-fabsf(z)));
;         run += ls * (1.f / 16.f); bl[i] = run; }
	v_mov_b32_e32 v136, v126
	s_waitcnt lgkmcnt(0)
	v_mov_b32_e32 v137, v132
	v_mov_b32_e32 v132, v127
	v_pk_mul_f32 v[126:127], v[6:7], v[132:133]
	v_mov_b32_e32 v132, v128
	v_pk_fma_f32 v[126:127], v[2:3], v[136:137], v[126:127]
	v_mov_b32_e32 v133, v134
	v_pk_fma_f32 v[126:127], v[4:5], v[132:133], v[126:127]
	v_mov_b32_e32 v134, v129
	v_pk_fma_f32 v[126:127], v[58:59], v[134:135], v[126:127]
	s_nop 0
	v_add_f32_e32 v125, v121, v126
	v_add_f32_e32 v125, v125, v127
	ds_read_b128 v[126:129], v13 offset:224
	ds_read_b128 v[132:135], v13 offset:240
	s_waitcnt lgkmcnt(1)
	v_mov_b32_e32 v136, v126
	s_waitcnt lgkmcnt(0)
	v_mov_b32_e32 v137, v132
	v_mov_b32_e32 v132, v127
	v_pk_mul_f32 v[126:127], v[64:65], v[132:133]
	v_mov_b32_e32 v132, v128
	v_pk_fma_f32 v[126:127], v[60:61], v[136:137], v[126:127]
	v_mov_b32_e32 v133, v134
	v_pk_fma_f32 v[126:127], v[62:63], v[132:133], v[126:127]
	v_mov_b32_e32 v134, v129
	v_pk_fma_f32 v[126:127], v[66:67], v[134:135], v[126:127]
	s_nop 0
	v_add_f32_e32 v125, v125, v126
	v_add_f32_e32 v125, v125, v127
	v_min_f32_e32 v126, 0, v125
	v_mul_f32_e64 v125, |v125|, s50
	v_exp_f32_e32 v125, v125
	s_nop 0
	v_add_f32_e32 v125, 1.0, v125
	v_cmp_gt_f32_e32 vcc, s51, v125
	s_nop 1
	v_cndmask_b32_e64 v127, 0, 32, vcc
	v_ldexp_f32 v125, v125, v127
	v_log_f32_e32 v125, v125
	s_nop 0
	v_mul_f32_e32 v127, 0x3f317217, v125
	v_fma_f32 v127, v125, s52, -v127
	v_fmac_f32_e32 v127, 0x3377d1cf, v125
	v_fmac_f32_e32 v127, 0x3f317217, v125
	v_cmp_lt_f32_e64 s[0:1], |v125|, s53
	s_nop 1
	v_cndmask_b32_e64 v125, v125, v127, s[0:1]
	v_cndmask_b32_e32 v127, 0, v88, vcc
	v_sub_f32_e32 v125, v125, v127
	v_sub_f32_e32 v125, v126, v125
	ds_read_b128 v[126:129], v13 offset:256
	ds_read_b128 v[132:135], v13 offset:272
	v_fmamk_f32 v125, v125, 0x3d800000, v124
	s_waitcnt lgkmcnt(1)
	v_mov_b32_e32 v136, v126
	s_waitcnt lgkmcnt(0)
	v_mov_b32_e32 v137, v132
	v_mov_b32_e32 v132, v127
	v_pk_mul_f32 v[126:127], v[6:7], v[132:133]
	v_mov_b32_e32 v132, v128
	v_pk_fma_f32 v[126:127], v[2:3], v[136:137], v[126:127]
	v_mov_b32_e32 v133, v134
	v_pk_fma_f32 v[126:127], v[4:5], v[132:133], v[126:127]
	v_mov_b32_e32 v134, v129
	v_pk_fma_f32 v[126:127], v[58:59], v[134:135], v[126:127]
	s_nop 0
	v_add_f32_e32 v126, v121, v126
	v_add_f32_e32 v138, v126, v127
	ds_read_b128 v[126:129], v13 offset:288
	ds_read_b128 v[132:135], v13 offset:304
	s_waitcnt lgkmcnt(1)
	v_mov_b32_e32 v136, v126
	s_waitcnt lgkmcnt(0)
	v_mov_b32_e32 v137, v132
	v_mov_b32_e32 v132, v127
	v_pk_mul_f32 v[126:127], v[64:65], v[132:133]
	v_mov_b32_e32 v132, v128
	v_pk_fma_f32 v[126:127], v[60:61], v[136:137], v[126:127]
	v_mov_b32_e32 v133, v134
	v_pk_fma_f32 v[126:127], v[62:63], v[132:133], v[126:127]
	v_mov_b32_e32 v134, v129
	v_pk_fma_f32 v[126:127], v[66:67], v[134:135], v[126:127]
	s_nop 0
	v_add_f32_e32 v126, v138, v126
	v_add_f32_e32 v126, v126, v127
	v_min_f32_e32 v127, 0, v126
	v_mul_f32_e64 v126, |v126|, s50
	v_exp_f32_e32 v126, v126
	ds_read_b128 v[132:135], v13 offset:320
	ds_read_b128 v[136:139], v13 offset:336
	v_add_f32_e32 v126, 1.0, v126
	v_cmp_gt_f32_e32 vcc, s51, v126
	s_waitcnt lgkmcnt(0)
	v_mov_b32_e32 v129, v136
	v_mov_b32_e32 v136, v133
	v_cndmask_b32_e64 v128, 0, 32, vcc
	v_ldexp_f32 v126, v126, v128
	v_log_f32_e32 v126, v126
	s_nop 0
	v_mul_f32_e32 v128, 0x3f317217, v126
	v_fma_f32 v128, v126, s52, -v128
	v_fmac_f32_e32 v128, 0x3377d1cf, v126
	v_fmac_f32_e32 v128, 0x3f317217, v126
	v_cmp_lt_f32_e64 s[0:1], |v126|, s53
	s_nop 1
	v_cndmask_b32_e64 v126, v126, v128, s[0:1]
	v_cndmask_b32_e32 v128, 0, v88, vcc
	v_sub_f32_e32 v126, v126, v128
	v_mov_b32_e32 v128, v132
	v_pk_mul_f32 v[132:133], v[6:7], v[136:137]
	v_sub_f32_e32 v126, v127, v126
	v_pk_fma_f32 v[128:129], v[2:3], v[128:129], v[132:133]
	v_mov_b32_e32 v132, v134
	v_mov_b32_e32 v133, v138
	v_pk_fma_f32 v[128:129], v[4:5], v[132:133], v[128:129]
	v_mov_b32_e32 v138, v135
	v_pk_fma_f32 v[128:129], v[58:59], v[138:139], v[128:129]
	ds_read_b128 v[132:135], v13 offset:352
	ds_read_b128 v[136:139], v13 offset:368
	v_add_f32_e32 v127, v121, v128
	v_add_f32_e32 v127, v127, v129
	v_fmamk_f32 v126, v126, 0x3d800000, v125
	s_waitcnt lgkmcnt(1)
	v_mov_b32_e32 v128, v132
	s_waitcnt lgkmcnt(0)
	v_mov_b32_e32 v129, v136
	v_mov_b32_e32 v136, v133
	v_pk_mul_f32 v[132:133], v[64:65], v[136:137]
	s_nop 0
	v_pk_fma_f32 v[128:129], v[60:61], v[128:129], v[132:133]
	v_mov_b32_e32 v132, v134
	v_mov_b32_e32 v133, v138
	v_pk_fma_f32 v[128:129], v[62:63], v[132:133], v[128:129]
	v_mov_b32_e32 v138, v135
	v_pk_fma_f32 v[128:129], v[66:67], v[138:139], v[128:129]
	ds_read_b128 v[132:135], v13 offset:384
	ds_read_b128 v[136:139], v13 offset:400
	v_add_f32_e32 v127, v127, v128
	v_add_f32_e32 v127, v127, v129
	v_min_f32_e32 v128, 0, v127
	v_mul_f32_e64 v127, |v127|, s50
	v_exp_f32_e32 v127, v127
	s_nop 0
	v_add_f32_e32 v127, 1.0, v127
	v_cmp_gt_f32_e32 vcc, s51, v127
	s_nop 1
	v_cndmask_b32_e64 v129, 0, 32, vcc
	v_ldexp_f32 v127, v127, v129
	v_log_f32_e32 v127, v127
	s_nop 0
	v_mul_f32_e32 v129, 0x3f317217, v127
	v_fma_f32 v129, v127, s52, -v129
	v_fmac_f32_e32 v129, 0x3377d1cf, v127
	v_fmac_f32_e32 v129, 0x3f317217, v127
	v_cmp_lt_f32_e64 s[0:1], |v127|, s53
	s_nop 1
	v_cndmask_b32_e64 v127, v127, v129, s[0:1]
	v_cndmask_b32_e32 v129, 0, v88, vcc
	v_sub_f32_e32 v127, v127, v129
	s_waitcnt lgkmcnt(0)
	v_mov_b32_e32 v129, v136
	v_mov_b32_e32 v136, v133
	v_sub_f32_e32 v127, v128, v127
	v_mov_b32_e32 v128, v132
	v_pk_mul_f32 v[132:133], v[6:7], v[136:137]
	v_fmamk_f32 v127, v127, 0x3d800000, v126
	v_pk_fma_f32 v[128:129], v[2:3], v[128:129], v[132:133]
	v_mov_b32_e32 v132, v134
	v_mov_b32_e32 v133, v138
	v_pk_fma_f32 v[128:129], v[4:5], v[132:133], v[128:129]
	v_mov_b32_e32 v138, v135
	v_pk_fma_f32 v[128:129], v[58:59], v[138:139], v[128:129]
	ds_read_b128 v[132:135], v13 offset:416
	ds_read_b128 v[136:139], v13 offset:432
	v_add_f32_e32 v128, v121, v128
	v_add_f32_e32 v140, v128, v129
	s_waitcnt lgkmcnt(1)
; #define LAS __attribute__((address_space(3)))
; __device__ __forceinline__ void gla_prep_unit(Frame& F, int unit) {
;     ...
;     for (int i = 0; i < 16; ++i) { const int c = cg * 16 + i; float z = bias;
; #pragma unroll
;         for (int r4 = 0; r4 < 4; ++r4) { const f32x4 g4 = *(const LAS f32x4*)(gaS + c * 16 + 4 * r4); z += g4.x * w2r[4 * r4] + g4.y * w2r[4 * r4 + 1] + g4.z * w2r[4 * r4 + 2] + g4.w * w2r[4 * r4 + 3]; }
;         const float ls = fminf(z, 0.f) - __logf(1.0f + __expf(-fabsf(z)));
;         run += ls * (1.f / 16.f); bl[i] = run; }
	v_mov_b32_e32 v128, v132
	s_waitcnt lgkmcnt(0)
	v_mov_b32_e32 v129, v136
	v_mov_b32_e32 v136, v133
	v_pk_mul_f32 v[132:133], v[64:65], v[136:137]
	s_nop 0
	v_pk_fma_f32 v[128:129], v[60:61], v[128:129], v[132:133]
	v_mov_b32_e32 v132, v134
	v_mov_b32_e32 v133, v138
	v_pk_fma_f32 v[128:129], v[62:63], v[132:133], v[128:129]
	v_mov_b32_e32 v138, v135
	v_pk_fma_f32 v[128:129], v[66:67], v[138:139], v[128:129]
	s_nop 0
	v_add_f32_e32 v128, v140, v128
	v_add_f32_e32 v128, v128, v129
	v_min_f32_e32 v129, 0, v128
	v_mul_f32_e64 v128, |v128|, s50
	v_exp_f32_e32 v128, v128
	s_nop 0
	v_add_f32_e32 v128, 1.0, v128
	v_cmp_gt_f32_e32 vcc, s51, v128
	s_nop 1
	v_cndmask_b32_e64 v132, 0, 32, vcc
	v_ldexp_f32 v128, v128, v132
	v_log_f32_e32 v128, v128
	s_nop 0
	v_mul_f32_e32 v132, 0x3f317217, v128
	v_fma_f32 v132, v128, s52, -v132
	v_fmac_f32_e32 v132, 0x3377d1cf, v128
	v_fmac_f32_e32 v132, 0x3f317217, v128
	v_cmp_lt_f32_e64 s[0:1], |v128|, s53
	s_nop 1
	v_cndmask_b32_e64 v128, v128, v132, s[0:1]
	v_cndmask_b32_e32 v132, 0, v88, vcc
	v_sub_f32_e32 v128, v128, v132
	ds_read_b128 v[132:135], v13 offset:448
	ds_read_b128 v[136:139], v13 offset:464
	v_sub_f32_e32 v128, v129, v128
	v_fmamk_f32 v128, v128, 0x3d800000, v127
	s_waitcnt lgkmcnt(1)
	v_mov_b32_e32 v140, v132
	s_waitcnt lgkmcnt(0)
	v_mov_b32_e32 v141, v136
	v_mov_b32_e32 v136, v133
	v_pk_mul_f32 v[132:133], v[6:7], v[136:137]
	v_mov_b32_e32 v136, v134
	v_pk_fma_f32 v[132:133], v[2:3], v[140:141], v[132:133]
	v_mov_b32_e32 v137, v138
	v_pk_fma_f32 v[132:133], v[4:5], v[136:137], v[132:133]
	v_mov_b32_e32 v138, v135
	v_pk_fma_f32 v[132:133], v[58:59], v[138:139], v[132:133]
	s_nop 0
	v_add_f32_e32 v129, v121, v132
	v_add_f32_e32 v129, v129, v133
	ds_read_b128 v[132:135], v13 offset:480
	ds_read_b128 v[136:139], v13 offset:496
	s_waitcnt lgkmcnt(1)
	v_mov_b32_e32 v140, v132
	s_waitcnt lgkmcnt(0)
	v_mov_b32_e32 v141, v136
	v_mov_b32_e32 v136, v133
	v_pk_mul_f32 v[132:133], v[64:65], v[136:137]
	v_mov_b32_e32 v136, v134
	v_pk_fma_f32 v[132:133], v[60:61], v[140:141], v[132:133]
	v_mov_b32_e32 v137, v138
	v_pk_fma_f32 v[132:133], v[62:63], v[136:137], v[132:133]
	v_mov_b32_e32 v138, v135
	v_pk_fma_f32 v[132:133], v[66:67], v[138:139], v[132:133]
	s_nop 0
	v_add_f32_e32 v129, v129, v132
	v_add_f32_e32 v129, v129, v133
	v_min_f32_e32 v132, 0, v129
	v_mul_f32_e64 v129, |v129|, s50
	v_exp_f32_e32 v129, v129
	s_nop 0
	v_add_f32_e32 v129, 1.0, v129
	v_cmp_gt_f32_e32 vcc, s51, v129
	s_nop 1
	v_cndmask_b32_e64 v133, 0, 32, vcc
	v_ldexp_f32 v129, v129, v133
	v_log_f32_e32 v129, v129
	s_nop 0
	v_mul_f32_e32 v133, 0x3f317217, v129
	v_fma_f32 v133, v129, s52, -v133
	v_fmac_f32_e32 v133, 0x3377d1cf, v129
	v_fmac_f32_e32 v133, 0x3f317217, v129
	v_cmp_lt_f32_e64 s[0:1], |v129|, s53
	s_nop 1
	v_cndmask_b32_e64 v129, v129, v133, s[0:1]
	v_cndmask_b32_e32 v133, 0, v88, vcc
	v_sub_f32_e32 v129, v129, v133
	v_sub_f32_e32 v129, v132, v129
	ds_read_b128 v[132:135], v13 offset:512
	ds_read_b128 v[136:139], v13 offset:528
	v_fmamk_f32 v129, v129, 0x3d800000, v128
	s_waitcnt lgkmcnt(1)
	v_mov_b32_e32 v140, v132
	s_waitcnt lgkmcnt(0)
	v_mov_b32_e32 v141, v136
	v_mov_b32_e32 v136, v133
	v_pk_mul_f32 v[132:133], v[6:7], v[136:137]
	v_mov_b32_e32 v136, v134
	v_pk_fma_f32 v[132:133], v[2:3], v[140:141], v[132:133]
	v_mov_b32_e32 v137, v138
	v_pk_fma_f32 v[132:133], v[4:5], v[136:137], v[132:133]
	v_mov_b32_e32 v138, v135
	v_pk_fma_f32 v[132:133], v[58:59], v[138:139], v[132:133]
	s_nop 0
	v_add_f32_e32 v132, v121, v132
	v_add_f32_e32 v142, v132, v133
	ds_read_b128 v[132:135], v13 offset:544
	ds_read_b128 v[136:139], v13 offset:560
	s_waitcnt lgkmcnt(1)
	v_mov_b32_e32 v140, v132
	s_waitcnt lgkmcnt(0)
	v_mov_b32_e32 v141, v136
	v_mov_b32_e32 v136, v133
	v_pk_mul_f32 v[132:133], v[64:65], v[136:137]
	v_mov_b32_e32 v136, v134
	v_pk_fma_f32 v[132:133], v[60:61], v[140:141], v[132:133]
	v_mov_b32_e32 v137, v138
	v_pk_fma_f32 v[132:133], v[62:63], v[136:137], v[132:133]
	v_mov_b32_e32 v138, v135
	v_pk_fma_f32 v[132:133], v[66:67], v[138:139], v[132:133]
	s_nop 0
	v_add_f32_e32 v132, v142, v132
	v_add_f32_e32 v132, v132, v133
	v_min_f32_e32 v133, 0, v132
	v_mul_f32_e64 v132, |v132|, s50
	v_exp_f32_e32 v132, v132
	s_nop 0
	v_add_f32_e32 v132, 1.0, v132
	v_cmp_gt_f32_e32 vcc, s51, v132
	s_nop 1
	v_cndmask_b32_e64 v134, 0, 32, vcc
	v_ldexp_f32 v132, v132, v134
	v_log_f32_e32 v132, v132
	s_nop 0
	v_mul_f32_e32 v134, 0x3f317217, v132
	v_fma_f32 v134, v132, s52, -v134
	v_fmac_f32_e32 v134, 0x3377d1cf, v132
	v_fmac_f32_e32 v134, 0x3f317217, v132
	v_cmp_lt_f32_e64 s[0:1], |v132|, s53
	s_nop 1
	v_cndmask_b32_e64 v132, v132, v134, s[0:1]
	v_cndmask_b32_e32 v134, 0, v88, vcc
	v_sub_f32_e32 v132, v132, v134
	ds_read_b128 v[134:137], v13 offset:576
	ds_read_b128 v[138:141], v13 offset:592
	v_sub_f32_e32 v132, v133, v132
	v_fmamk_f32 v132, v132, 0x3d800000, v129
	s_waitcnt lgkmcnt(1)
	v_mov_b32_e32 v142, v134
	s_waitcnt lgkmcnt(0)
	v_mov_b32_e32 v143, v138
	v_mov_b32_e32 v138, v135
	v_pk_mul_f32 v[134:135], v[6:7], v[138:139]
	v_mov_b32_e32 v138, v136
	v_pk_fma_f32 v[134:135], v[2:3], v[142:143], v[134:135]
	v_mov_b32_e32 v139, v140
	v_pk_fma_f32 v[134:135], v[4:5], v[138:139], v[134:135]
	v_mov_b32_e32 v140, v137
	v_pk_fma_f32 v[134:135], v[58:59], v[140:141], v[134:135]
	s_nop 0
	v_add_f32_e32 v133, v121, v134
	v_add_f32_e32 v133, v133, v135
	ds_read_b128 v[134:137], v13 offset:608
	ds_read_b128 v[138:141], v13 offset:624
	s_waitcnt lgkmcnt(1)
	v_mov_b32_e32 v142, v134
	s_waitcnt lgkmcnt(0)
; #define LAS __attribute__((address_space(3)))
; __device__ __forceinline__ void gla_prep_unit(Frame& F, int unit) {
;     ...
;     for (int i = 0; i < 16; ++i) { const int c = cg * 16 + i; float z = bias;
; #pragma unroll
;         for (int r4 = 0; r4 < 4; ++r4) { const f32x4 g4 = *(const LAS f32x4*)(gaS + c * 16 + 4 * r4); z += g4.x * w2r[4 * r4] + g4.y * w2r[4 * r4 + 1] + g4.z * w2r[4 * r4 + 2] + g4.w * w2r[4 * r4 + 3]; }
;         const float ls = fminf(z, 0.f) - __logf(1.0f + __expf(-fabsf(z)));
;         run += ls * (1.f / 16.f); bl[i] = run; }
	v_mov_b32_e32 v143, v138
	v_mov_b32_e32 v138, v135
	v_pk_mul_f32 v[134:135], v[64:65], v[138:139]
	v_mov_b32_e32 v138, v136
	v_pk_fma_f32 v[134:135], v[60:61], v[142:143], v[134:135]
	v_mov_b32_e32 v139, v140
	v_pk_fma_f32 v[134:135], v[62:63], v[138:139], v[134:135]
	v_mov_b32_e32 v140, v137
	v_pk_fma_f32 v[134:135], v[66:67], v[140:141], v[134:135]
	s_nop 0
	v_add_f32_e32 v133, v133, v134
	v_add_f32_e32 v133, v133, v135
	v_min_f32_e32 v134, 0, v133
	v_mul_f32_e64 v133, |v133|, s50
	v_exp_f32_e32 v133, v133
	s_nop 0
	v_add_f32_e32 v133, 1.0, v133
	v_cmp_gt_f32_e32 vcc, s51, v133
	s_nop 1
	v_cndmask_b32_e64 v135, 0, 32, vcc
	v_ldexp_f32 v133, v133, v135
	v_log_f32_e32 v133, v133
	s_nop 0
	v_mul_f32_e32 v135, 0x3f317217, v133
	v_fma_f32 v135, v133, s52, -v135
	v_fmac_f32_e32 v135, 0x3377d1cf, v133
	v_fmac_f32_e32 v135, 0x3f317217, v133
	v_cmp_lt_f32_e64 s[0:1], |v133|, s53
	s_nop 1
	v_cndmask_b32_e64 v133, v133, v135, s[0:1]
	v_cndmask_b32_e32 v135, 0, v88, vcc
	v_sub_f32_e32 v133, v133, v135
	v_sub_f32_e32 v133, v134, v133
	ds_read_b128 v[134:137], v13 offset:640
	ds_read_b128 v[138:141], v13 offset:656
	v_fmamk_f32 v133, v133, 0x3d800000, v132
	s_waitcnt lgkmcnt(1)
	v_mov_b32_e32 v142, v134
	s_waitcnt lgkmcnt(0)
	v_mov_b32_e32 v143, v138
	v_mov_b32_e32 v138, v135
	v_pk_mul_f32 v[134:135], v[6:7], v[138:139]
	v_mov_b32_e32 v138, v136
	v_pk_fma_f32 v[134:135], v[2:3], v[142:143], v[134:135]
	v_mov_b32_e32 v139, v140
	v_pk_fma_f32 v[134:135], v[4:5], v[138:139], v[134:135]
	v_mov_b32_e32 v140, v137
	v_pk_fma_f32 v[134:135], v[58:59], v[140:141], v[134:135]
	s_nop 0
	v_add_f32_e32 v134, v121, v134
	v_add_f32_e32 v144, v134, v135
	ds_read_b128 v[134:137], v13 offset:672
	ds_read_b128 v[138:141], v13 offset:688
	s_waitcnt lgkmcnt(1)
	v_mov_b32_e32 v142, v134
	s_waitcnt lgkmcnt(0)
	v_mov_b32_e32 v143, v138
	v_mov_b32_e32 v138, v135
	v_pk_mul_f32 v[134:135], v[64:65], v[138:139]
	v_mov_b32_e32 v138, v136
	v_pk_fma_f32 v[134:135], v[60:61], v[142:143], v[134:135]
	v_mov_b32_e32 v139, v140
	v_pk_fma_f32 v[134:135], v[62:63], v[138:139], v[134:135]
	v_mov_b32_e32 v140, v137
	v_pk_fma_f32 v[134:135], v[66:67], v[140:141], v[134:135]
	s_nop 0
	v_add_f32_e32 v134, v144, v134
	v_add_f32_e32 v134, v134, v135
	v_min_f32_e32 v135, 0, v134
	v_mul_f32_e64 v134, |v134|, s50
	v_exp_f32_e32 v134, v134
	s_nop 0
	v_add_f32_e32 v134, 1.0, v134
	v_cmp_gt_f32_e32 vcc, s51, v134
	s_nop 1
	v_cndmask_b32_e64 v136, 0, 32, vcc
	v_ldexp_f32 v134, v134, v136
	v_log_f32_e32 v134, v134
	s_nop 0
	v_mul_f32_e32 v136, 0x3f317217, v134
	v_fma_f32 v136, v134, s52, -v136
	v_fmac_f32_e32 v136, 0x3377d1cf, v134
	v_fmac_f32_e32 v136, 0x3f317217, v134
	v_cmp_lt_f32_e64 s[0:1], |v134|, s53
	s_nop 1
	v_cndmask_b32_e64 v134, v134, v136, s[0:1]
	v_cndmask_b32_e32 v136, 0, v88, vcc
	v_sub_f32_e32 v134, v134, v136
	ds_read_b128 v[136:139], v13 offset:704
	ds_read_b128 v[140:143], v13 offset:720
	v_sub_f32_e32 v134, v135, v134
	v_fmamk_f32 v134, v134, 0x3d800000, v133
	s_waitcnt lgkmcnt(1)
	v_mov_b32_e32 v144, v136
	s_waitcnt lgkmcnt(0)
	v_mov_b32_e32 v145, v140
	v_mov_b32_e32 v140, v137
	v_pk_mul_f32 v[136:137], v[6:7], v[140:141]
	v_mov_b32_e32 v140, v138
	v_pk_fma_f32 v[136:137], v[2:3], v[144:145], v[136:137]
	v_mov_b32_e32 v141, v142
	v_pk_fma_f32 v[136:137], v[4:5], v[140:141], v[136:137]
	v_mov_b32_e32 v142, v139
	v_pk_fma_f32 v[136:137], v[58:59], v[142:143], v[136:137]
	s_nop 0
	v_add_f32_e32 v135, v121, v136
	v_add_f32_e32 v135, v135, v137
	ds_read_b128 v[136:139], v13 offset:736
	ds_read_b128 v[140:143], v13 offset:752
	s_waitcnt lgkmcnt(1)
	v_mov_b32_e32 v144, v136
	s_waitcnt lgkmcnt(0)
	v_mov_b32_e32 v145, v140
	v_mov_b32_e32 v140, v137
	v_pk_mul_f32 v[136:137], v[64:65], v[140:141]
	v_mov_b32_e32 v140, v138
	v_pk_fma_f32 v[136:137], v[60:61], v[144:145], v[136:137]
	v_mov_b32_e32 v141, v142
	v_pk_fma_f32 v[136:137], v[62:63], v[140:141], v[136:137]
	v_mov_b32_e32 v142, v139
	v_pk_fma_f32 v[136:137], v[66:67], v[142:143], v[136:137]
	s_nop 0
	v_add_f32_e32 v135, v135, v136
	v_add_f32_e32 v135, v135, v137
	v_min_f32_e32 v136, 0, v135
	v_mul_f32_e64 v135, |v135|, s50
	v_exp_f32_e32 v135, v135
	s_nop 0
	v_add_f32_e32 v135, 1.0, v135
	v_cmp_gt_f32_e32 vcc, s51, v135
	s_nop 1
	v_cndmask_b32_e64 v137, 0, 32, vcc
	v_ldexp_f32 v135, v135, v137
	v_log_f32_e32 v135, v135
	s_nop 0
	v_mul_f32_e32 v137, 0x3f317217, v135
	v_fma_f32 v137, v135, s52, -v137
	v_fmac_f32_e32 v137, 0x3377d1cf, v135
	v_fmac_f32_e32 v137, 0x3f317217, v135
	v_cmp_lt_f32_e64 s[0:1], |v135|, s53
	s_nop 1
	v_cndmask_b32_e64 v135, v135, v137, s[0:1]
	v_cndmask_b32_e32 v137, 0, v88, vcc
	v_sub_f32_e32 v135, v135, v137
	v_sub_f32_e32 v135, v136, v135
	ds_read_b128 v[136:139], v13 offset:768
	ds_read_b128 v[140:143], v13 offset:784
	v_fmamk_f32 v135, v135, 0x3d800000, v134
	s_waitcnt lgkmcnt(1)
	v_mov_b32_e32 v144, v136
	s_waitcnt lgkmcnt(0)
	v_mov_b32_e32 v145, v140
	v_mov_b32_e32 v140, v137
	v_pk_mul_f32 v[136:137], v[6:7], v[140:141]
	v_mov_b32_e32 v140, v138
	v_pk_fma_f32 v[136:137], v[2:3], v[144:145], v[136:137]
	v_mov_b32_e32 v141, v142
	v_pk_fma_f32 v[136:137], v[4:5], v[140:141], v[136:137]
	v_mov_b32_e32 v142, v139
	v_pk_fma_f32 v[136:137], v[58:59], v[142:143], v[136:137]
	s_nop 0
	v_add_f32_e32 v136, v121, v136
	v_add_f32_e32 v146, v136, v137
	ds_read_b128 v[136:139], v13 offset:800
	ds_read_b128 v[140:143], v13 offset:816
	s_waitcnt lgkmcnt(1)
	v_mov_b32_e32 v144, v136
	s_waitcnt lgkmcnt(0)
; #define LAS __attribute__((address_space(3)))
; __device__ __forceinline__ void gla_prep_unit(Frame& F, int unit) {
;     ...
;     for (int i = 0; i < 16; ++i) { const int c = cg * 16 + i; float z = bias;
; #pragma unroll
;         for (int r4 = 0; r4 < 4; ++r4) { const f32x4 g4 = *(const LAS f32x4*)(gaS + c * 16 + 4 * r4); z += g4.x * w2r[4 * r4] + g4.y * w2r[4 * r4 + 1] + g4.z * w2r[4 * r4 + 2] + g4.w * w2r[4 * r4 + 3]; }
;         const float ls = fminf(z, 0.f) - __logf(1.0f + __expf(-fabsf(z)));
;         run += ls * (1.f / 16.f); bl[i] = run; }
;     tot[cg * 128 + d] = run;
;     __syncthreads();
	v_mov_b32_e32 v145, v140
	v_mov_b32_e32 v140, v137
	v_pk_mul_f32 v[136:137], v[64:65], v[140:141]
	v_mov_b32_e32 v140, v138
	v_pk_fma_f32 v[136:137], v[60:61], v[144:145], v[136:137]
	v_mov_b32_e32 v141, v142
	v_pk_fma_f32 v[136:137], v[62:63], v[140:141], v[136:137]
	v_mov_b32_e32 v142, v139
	v_pk_fma_f32 v[136:137], v[66:67], v[142:143], v[136:137]
	s_nop 0
	v_add_f32_e32 v136, v146, v136
	v_add_f32_e32 v136, v136, v137
	v_min_f32_e32 v137, 0, v136
	v_mul_f32_e64 v136, |v136|, s50
	v_exp_f32_e32 v136, v136
	s_nop 0
	v_add_f32_e32 v136, 1.0, v136
	v_cmp_gt_f32_e32 vcc, s51, v136
	s_nop 1
	v_cndmask_b32_e64 v138, 0, 32, vcc
	v_ldexp_f32 v136, v136, v138
	v_log_f32_e32 v136, v136
	s_nop 0
	v_mul_f32_e32 v138, 0x3f317217, v136
	v_fma_f32 v138, v136, s52, -v138
	v_fmac_f32_e32 v138, 0x3377d1cf, v136
	v_fmac_f32_e32 v138, 0x3f317217, v136
	v_cmp_lt_f32_e64 s[0:1], |v136|, s53
	s_nop 1
	v_cndmask_b32_e64 v136, v136, v138, s[0:1]
	v_cndmask_b32_e32 v138, 0, v88, vcc
	v_sub_f32_e32 v136, v136, v138
	ds_read_b128 v[138:141], v13 offset:832
	ds_read_b128 v[142:145], v13 offset:848
	v_sub_f32_e32 v136, v137, v136
	v_fmamk_f32 v136, v136, 0x3d800000, v135
	s_waitcnt lgkmcnt(1)
	v_mov_b32_e32 v146, v138
	s_waitcnt lgkmcnt(0)
	v_mov_b32_e32 v147, v142
	v_mov_b32_e32 v142, v139
	v_pk_mul_f32 v[138:139], v[6:7], v[142:143]
	v_mov_b32_e32 v142, v140
	v_pk_fma_f32 v[138:139], v[2:3], v[146:147], v[138:139]
	v_mov_b32_e32 v143, v144
	v_pk_fma_f32 v[138:139], v[4:5], v[142:143], v[138:139]
	v_mov_b32_e32 v144, v141
	v_pk_fma_f32 v[138:139], v[58:59], v[144:145], v[138:139]
	s_nop 0
	v_add_f32_e32 v137, v121, v138
	v_add_f32_e32 v137, v137, v139
	ds_read_b128 v[138:141], v13 offset:864
	ds_read_b128 v[142:145], v13 offset:880
	s_waitcnt lgkmcnt(1)
	v_mov_b32_e32 v146, v138
	s_waitcnt lgkmcnt(0)
	v_mov_b32_e32 v147, v142
	v_mov_b32_e32 v142, v139
	v_pk_mul_f32 v[138:139], v[64:65], v[142:143]
	v_mov_b32_e32 v142, v140
	v_pk_fma_f32 v[138:139], v[60:61], v[146:147], v[138:139]
	v_mov_b32_e32 v143, v144
	v_pk_fma_f32 v[138:139], v[62:63], v[142:143], v[138:139]
	v_mov_b32_e32 v144, v141
	v_pk_fma_f32 v[138:139], v[66:67], v[144:145], v[138:139]
	s_nop 0
	v_add_f32_e32 v137, v137, v138
	v_add_f32_e32 v137, v137, v139
	v_min_f32_e32 v138, 0, v137
	v_mul_f32_e64 v137, |v137|, s50
	v_exp_f32_e32 v137, v137
	s_nop 0
	v_add_f32_e32 v137, 1.0, v137
	v_cmp_gt_f32_e32 vcc, s51, v137
	s_nop 1
	v_cndmask_b32_e64 v139, 0, 32, vcc
	v_ldexp_f32 v137, v137, v139
	v_log_f32_e32 v137, v137
	s_nop 0
	v_mul_f32_e32 v139, 0x3f317217, v137
	v_fma_f32 v139, v137, s52, -v139
	v_fmac_f32_e32 v139, 0x3377d1cf, v137
	v_fmac_f32_e32 v139, 0x3f317217, v137
	v_cmp_lt_f32_e64 s[0:1], |v137|, s53
	s_nop 1
	v_cndmask_b32_e64 v137, v137, v139, s[0:1]
	v_cndmask_b32_e32 v139, 0, v88, vcc
	v_sub_f32_e32 v137, v137, v139
	v_sub_f32_e32 v137, v138, v137
	ds_read_b128 v[138:141], v13 offset:896
	ds_read_b128 v[142:145], v13 offset:912
	v_fmamk_f32 v137, v137, 0x3d800000, v136
	s_waitcnt lgkmcnt(1)
	v_mov_b32_e32 v146, v138
	s_waitcnt lgkmcnt(0)
	v_mov_b32_e32 v147, v142
	v_mov_b32_e32 v142, v139
	v_pk_mul_f32 v[138:139], v[6:7], v[142:143]
	v_mov_b32_e32 v142, v140
	v_pk_fma_f32 v[138:139], v[2:3], v[146:147], v[138:139]
	v_mov_b32_e32 v143, v144
	v_pk_fma_f32 v[138:139], v[4:5], v[142:143], v[138:139]
	v_mov_b32_e32 v144, v141
	v_pk_fma_f32 v[138:139], v[58:59], v[144:145], v[138:139]
	s_nop 0
	v_add_f32_e32 v138, v121, v138
	v_add_f32_e32 v148, v138, v139
	ds_read_b128 v[138:141], v13 offset:928
	ds_read_b128 v[142:145], v13 offset:944
	s_waitcnt lgkmcnt(1)
	v_mov_b32_e32 v146, v138
	s_waitcnt lgkmcnt(0)
	v_mov_b32_e32 v147, v142
	v_mov_b32_e32 v142, v139
	v_pk_mul_f32 v[138:139], v[64:65], v[142:143]
	v_mov_b32_e32 v142, v140
	v_pk_fma_f32 v[138:139], v[60:61], v[146:147], v[138:139]
	v_mov_b32_e32 v143, v144
	v_pk_fma_f32 v[138:139], v[62:63], v[142:143], v[138:139]
	v_mov_b32_e32 v144, v141
	v_pk_fma_f32 v[138:139], v[66:67], v[144:145], v[138:139]
	s_nop 0
	v_add_f32_e32 v138, v148, v138
	v_add_f32_e32 v138, v138, v139
	v_min_f32_e32 v139, 0, v138
	v_mul_f32_e64 v138, |v138|, s50
	v_exp_f32_e32 v138, v138
	s_nop 0
	v_add_f32_e32 v138, 1.0, v138
	v_cmp_gt_f32_e32 vcc, s51, v138
	s_nop 1
	v_cndmask_b32_e64 v140, 0, 32, vcc
	v_ldexp_f32 v138, v138, v140
	v_log_f32_e32 v138, v138
	s_nop 0
	v_mul_f32_e32 v140, 0x3f317217, v138
	v_fma_f32 v140, v138, s52, -v140
	v_fmac_f32_e32 v140, 0x3377d1cf, v138
	v_fmac_f32_e32 v140, 0x3f317217, v138
	v_cmp_lt_f32_e64 s[0:1], |v138|, s53
	s_nop 1
	v_cndmask_b32_e64 v138, v138, v140, s[0:1]
	v_cndmask_b32_e32 v140, 0, v88, vcc
	v_sub_f32_e32 v138, v138, v140
	ds_read_b128 v[140:143], v13 offset:960
	ds_read_b128 v[144:147], v13 offset:976
	v_sub_f32_e32 v138, v139, v138
	v_fmamk_f32 v138, v138, 0x3d800000, v137
	s_waitcnt lgkmcnt(1)
	v_mov_b32_e32 v148, v140
	s_waitcnt lgkmcnt(0)
	v_mov_b32_e32 v149, v144
	v_mov_b32_e32 v144, v141
	v_pk_mul_f32 v[6:7], v[6:7], v[144:145]
	s_nop 0
	v_pk_fma_f32 v[2:3], v[2:3], v[148:149], v[6:7]
	v_mov_b32_e32 v6, v142
	v_mov_b32_e32 v7, v146
	v_pk_fma_f32 v[2:3], v[4:5], v[6:7], v[2:3]
	v_mov_b32_e32 v146, v143
	v_pk_fma_f32 v[2:3], v[58:59], v[146:147], v[2:3]
	s_nop 0
	v_add_f32_e32 v2, v121, v2
	v_add_f32_e32 v58, v2, v3
	ds_read_b128 v[2:5], v13 offset:992
	ds_read_b128 v[140:143], v13 offset:1008
	s_waitcnt lgkmcnt(1)
	v_mov_b32_e32 v6, v2
	s_waitcnt lgkmcnt(0)
	v_mov_b32_e32 v7, v140
	v_mov_b32_e32 v140, v3
	v_pk_mul_f32 v[2:3], v[64:65], v[140:141]
	s_nop 0
	v_pk_fma_f32 v[2:3], v[60:61], v[6:7], v[2:3]
	v_mov_b32_e32 v6, v4
	v_mov_b32_e32 v7, v142
	v_pk_fma_f32 v[2:3], v[62:63], v[6:7], v[2:3]
	v_mov_b32_e32 v142, v5
	v_pk_fma_f32 v[2:3], v[66:67], v[142:143], v[2:3]
	s_nop 0
	v_add_f32_e32 v2, v58, v2
	v_add_f32_e32 v2, v2, v3
	v_min_f32_e32 v3, 0, v2
	v_mul_f32_e64 v2, |v2|, s50
	v_exp_f32_e32 v2, v2
	v_lshl_add_u64 v[58:59], s[66:67], 0, v[28:29]
	v_add_f32_e32 v2, 1.0, v2
	v_cmp_gt_f32_e32 vcc, s51, v2
	s_nop 1
	v_cndmask_b32_e64 v4, 0, 32, vcc
	v_ldexp_f32 v2, v2, v4
	v_log_f32_e32 v2, v2
	s_nop 0
	v_mul_f32_e32 v4, 0x3f317217, v2
	v_fma_f32 v4, v2, s52, -v4
	v_fmac_f32_e32 v4, 0x3377d1cf, v2
	v_fmac_f32_e32 v4, 0x3f317217, v2
	v_cmp_lt_f32_e64 s[0:1], |v2|, s53
	s_nop 1
	v_cndmask_b32_e64 v2, v2, v4, s[0:1]
	v_cndmask_b32_e32 v4, 0, v88, vcc
	v_sub_f32_e32 v2, v2, v4
	v_sub_f32_e32 v2, v3, v2
	v_fmamk_f32 v3, v2, 0x3d800000, v138
	ds_write_b32 v68, v3 offset:4096
	s_waitcnt lgkmcnt(0)
	s_barrier
; __device__ __forceinline__ unsigned f2bf(float f) { unsigned u = __builtin_bit_cast(unsigned, f); return (u + 0x7fffu + ((u >> 16) & 1u)) >> 16; }
; __device__ __forceinline__ void gla_prep_unit(Frame& F, int unit) {
;     ...
;     float offs = 0.f, blast = 0.f;
; #pragma unroll
;     for (int g = 0; g < 4; ++g) { const float t = tot[g * 128 + d]; blast += t; if (g < cg) offs += t; }
;     const float eblast = __expf(blast);
;     unsigned kd[8];
; #pragma unroll
;     for (int i = 0; i < 16; i += 2) { float kdv[2];
; #pragma unroll
;         for (int u = 0; u < 2; ++u) { const int c = cg * 16 + i + u; const float bb = bl[i + u] + offs;
;             const float q = bf2f(qv[i + u]) * 0.08838834764831845f, k = bf2f(kv[i + u]);
;             const float eb = __expf(bb), einv = __builtin_amdgcn_rcpf(eb);
;             const float qin = q * eb, kin = k * einv; kdv[u] = kin * eblast;
;             const bf16_t qb16 = (bf16_t)f2bf(qin); qinS[c * GP_ROW + d] = qb16; kinS[c * GP_ROW + d] = (bf16_t)f2bf(kin); QIN[c * 128 + d] = qb16; }
	ds_read2st64_b32 v[4:5], v69 offset0:16 offset1:18
	s_waitcnt lgkmcnt(0)
	v_add_f32_e32 v2, 0, v4
	v_cndmask_b32_e64 v4, v2, 0, s[4:5]
	v_add_f32_e32 v2, v2, v5
	v_add_f32_e32 v5, v5, v4
	v_cndmask_b32_e64 v6, v4, v5, s[6:7]
	ds_read2st64_b32 v[4:5], v69 offset0:20 offset1:22
	s_waitcnt lgkmcnt(0)
	v_add_f32_e32 v2, v2, v4
	v_add_f32_e32 v4, v4, v6
	v_cndmask_b32_e64 v4, v6, v4, s[8:9]
	v_add_f32_e32 v2, v2, v5
	v_add_f32_e32 v5, v5, v4
	v_cndmask_b32_e64 v62, v4, v5, s[10:11]
	v_add_f32_e32 v4, v122, v62
	v_mul_f32_e32 v4, 0x3fb8aa3b, v4
	v_exp_f32_e32 v6, v4
	v_lshlrev_b32_e32 v5, 16, v120
	v_mul_f32_e32 v5, 0x3db504f3, v5
	v_mul_f32_e32 v2, 0x3fb8aa3b, v2
	v_mul_f32_e32 v5, v5, v6
	v_rcp_f32_e32 v4, v6
	v_bfe_u32 v6, v5, 16, 1
	v_add3_u32 v5, v5, v6, s55
	v_lshrrev_b32_e32 v5, 16, v5
	v_lshl_add_u64 v[6:7], s[66:67], 0, v[26:27]
	ds_write_b16 v70, v5 offset:8192
	global_store_short v[6:7], v5, off
	v_add_f32_e32 v5, v123, v62
	v_mul_f32_e32 v5, 0x3fb8aa3b, v5
	v_exp_f32_e32 v5, v5
	v_lshlrev_b32_e32 v6, 16, v119
	v_mul_f32_e32 v7, 0x3db504f3, v6
	v_exp_f32_e32 v2, v2
	v_rcp_f32_e32 v6, v5
	v_mul_f32_e32 v5, v7, v5
	v_bfe_u32 v7, v5, 16, 1
	v_add3_u32 v5, v5, v7, s55
	v_lshrrev_b32_e32 v60, 16, v5
	v_add_f32_e32 v5, v124, v62
	v_mul_f32_e32 v5, 0x3fb8aa3b, v5
	global_store_short v[58:59], v60, off
	v_exp_f32_e32 v58, v5
	v_lshlrev_b32_e32 v7, 16, v117
	v_mul_f32_e32 v7, 0x3db504f3, v7
	v_mul_f32_e32 v7, v7, v58
	v_rcp_f32_e32 v5, v58
	v_bfe_u32 v58, v7, 16, 1
	v_add3_u32 v7, v7, v58, s55
	v_lshrrev_b32_e32 v63, 16, v7
	v_add_f32_e32 v7, v125, v62
	v_lshl_add_u64 v[58:59], s[66:67], 0, v[30:31]
	v_mul_f32_e32 v7, 0x3fb8aa3b, v7
	global_store_short v[58:59], v63, off
	v_exp_f32_e32 v59, v7
	v_lshlrev_b32_e32 v58, 16, v118
	v_mul_f32_e32 v58, 0x3db504f3, v58
	v_mul_f32_e32 v58, v58, v59
	v_rcp_f32_e32 v7, v59
	v_bfe_u32 v59, v58, 16, 1
	v_add3_u32 v58, v58, v59, s55
	v_lshrrev_b32_e32 v64, 16, v58
	v_lshl_add_u64 v[58:59], s[66:67], 0, v[32:33]
	global_store_short v[58:59], v64, off
	v_lshlrev_b32_e32 v59, 16, v114
	v_lshlrev_b32_e32 v58, 16, v115
	v_pk_mul_f32 v[58:59], v[4:5], v[58:59]
	v_lshlrev_b32_e32 v5, 16, v112
	v_bfe_u32 v4, v58, 16, 1
	v_add3_u32 v4, v58, v4, s55
	ds_write_b16_d16_hi v70, v4 offset:25600
	ds_write_b16 v71, v60 offset:8192
	v_lshlrev_b32_e32 v4, 16, v111
	v_pk_mul_f32 v[60:61], v[6:7], v[4:5]
	v_bfe_u32 v6, v59, 16, 1
	v_bfe_u32 v4, v60, 16, 1
	v_add3_u32 v4, v60, v4, s55
	ds_write_b16_d16_hi v71, v4 offset:25600
	v_pk_mul_f32 v[4:5], v[2:3], v[58:59] op_sel_hi:[0,1]
	v_bfe_u32 v58, v61, 16, 1
	v_add3_u32 v58, v61, v58, s55
	ds_write_b16 v72, v63 offset:8192
	ds_write_b16_d16_hi v73, v58 offset:25600
	v_add_f32_e32 v58, v126, v62
	v_add3_u32 v6, v59, v6, s55
	v_mul_f32_e32 v58, 0x3fb8aa3b, v58
	ds_write_b16_d16_hi v72, v6 offset:25600
	v_pk_mul_f32 v[6:7], v[2:3], v[60:61] op_sel_hi:[0,1]
	v_exp_f32_e32 v60, v58
	v_lshlrev_b32_e32 v59, 16, v110
	v_mul_f32_e32 v59, 0x3db504f3, v59
	ds_write_b16 v73, v64 offset:8192
	v_mul_f32_e32 v59, v59, v60
	v_rcp_f32_e32 v58, v60
	v_bfe_u32 v60, v59, 16, 1
	v_add3_u32 v59, v59, v60, s55
	v_lshrrev_b32_e32 v59, 16, v59
	v_lshl_add_u64 v[60:61], s[66:67], 0, v[34:35]
	ds_write_b16 v74, v59 offset:8192
	global_store_short v[60:61], v59, off
	v_add_f32_e32 v59, v127, v62
	v_mul_f32_e32 v59, 0x3fb8aa3b, v59
	v_exp_f32_e32 v59, v59
	v_lshlrev_b32_e32 v60, 16, v109
	v_mul_f32_e32 v61, 0x3db504f3, v60
	v_lshl_add_u64 v[64:65], s[66:67], 0, v[36:37]
	v_rcp_f32_e32 v60, v59
	v_mul_f32_e32 v59, v61, v59
	v_bfe_u32 v61, v59, 16, 1
	v_add3_u32 v59, v59, v61, s55
	v_lshrrev_b32_e32 v63, 16, v59
	v_add_f32_e32 v59, v128, v62
	v_mul_f32_e32 v59, 0x3fb8aa3b, v59
	global_store_short v[64:65], v63, off
	v_exp_f32_e32 v64, v59
	v_lshlrev_b32_e32 v61, 16, v107
	v_mul_f32_e32 v61, 0x3db504f3, v61
	v_mul_f32_e32 v61, v61, v64
	v_rcp_f32_e32 v59, v64
	v_bfe_u32 v64, v61, 16, 1
	v_add3_u32 v61, v61, v64, s55
	v_lshrrev_b32_e32 v107, 16, v61
	v_add_f32_e32 v61, v129, v62
	v_lshl_add_u64 v[64:65], s[66:67], 0, v[38:39]
	v_mul_f32_e32 v61, 0x3fb8aa3b, v61
	global_store_short v[64:65], v107, off
	v_exp_f32_e32 v65, v61
	v_lshlrev_b32_e32 v64, 16, v104
	v_mul_f32_e32 v64, 0x3db504f3, v64
	v_mul_f32_e32 v64, v64, v65
	v_rcp_f32_e32 v61, v65
	v_bfe_u32 v65, v64, 16, 1
	v_add3_u32 v64, v64, v65, s55
	v_lshrrev_b32_e32 v104, 16, v64
	v_lshl_add_u64 v[64:65], s[66:67], 0, v[40:41]
	global_store_short v[64:65], v104, off
	v_lshlrev_b32_e32 v65, 16, v101
	v_lshlrev_b32_e32 v64, 16, v100
	v_pk_mul_f32 v[64:65], v[58:59], v[64:65]
	v_lshlrev_b32_e32 v59, 16, v105
	v_bfe_u32 v58, v64, 16, 1
	v_add3_u32 v58, v64, v58, s55
	ds_write_b16_d16_hi v74, v58 offset:25600
	ds_write_b16 v75, v63 offset:8192
	v_lshlrev_b32_e32 v58, 16, v102
	v_pk_mul_f32 v[66:67], v[60:61], v[58:59]
	v_bfe_u32 v60, v65, 16, 1
	v_bfe_u32 v58, v66, 16, 1
	v_bfe_u32 v63, v67, 16, 1
	v_add3_u32 v58, v66, v58, s55
	v_add3_u32 v60, v65, v60, s55
	v_add3_u32 v63, v67, v63, s55
	ds_write_b16_d16_hi v75, v58 offset:25600
	ds_write_b16 v76, v107 offset:8192
	ds_write_b16_d16_hi v76, v60 offset:25600
	ds_write_b16_d16_hi v77, v63 offset:25600
	v_add_f32_e32 v63, v132, v62
	v_mul_f32_e32 v63, 0x3fb8aa3b, v63
	v_exp_f32_e32 v63, v63
	v_pk_mul_f32 v[58:59], v[2:3], v[64:65] op_sel_hi:[0,1]
	v_lshlrev_b32_e32 v64, 16, v116
	v_mul_f32_e32 v65, 0x3db504f3, v64
	v_rcp_f32_e32 v64, v63
	v_mul_f32_e32 v63, v65, v63
	v_bfe_u32 v65, v63, 16, 1
	v_add3_u32 v63, v63, v65, s55
	v_pk_mul_f32 v[60:61], v[2:3], v[66:67] op_sel_hi:[0,1]
	v_lshrrev_b32_e32 v63, 16, v63
	v_lshl_add_u64 v[66:67], s[66:67], 0, v[42:43]
	ds_write_b16 v77, v104 offset:8192
; __device__ __forceinline__ unsigned f2bf(float f) { unsigned u = __builtin_bit_cast(unsigned, f); return (u + 0x7fffu + ((u >> 16) & 1u)) >> 16; }
; __device__ __forceinline__ unsigned pk2(float lo, float hi) { return f2bf(lo) | (f2bf(hi) << 16); }
; __device__ __forceinline__ void gla_prep_unit(Frame& F, int unit) {
;     ...
;     for (int i = 0; i < 16; i += 2) { float kdv[2];
; #pragma unroll
;         for (int u = 0; u < 2; ++u) { const int c = cg * 16 + i + u; const float bb = bl[i + u] + offs;
;             const float q = bf2f(qv[i + u]) * 0.08838834764831845f, k = bf2f(kv[i + u]);
;             const float eb = __expf(bb), einv = __builtin_amdgcn_rcpf(eb);
;             const float qin = q * eb, kin = k * einv; kdv[u] = kin * eblast;
;             const bf16_t qb16 = (bf16_t)f2bf(qin); qinS[c * GP_ROW + d] = qb16; kinS[c * GP_ROW + d] = (bf16_t)f2bf(kin); QIN[c * 128 + d] = qb16; }
;         kd[i >> 1] = pk2(kdv[0], kdv[1]); }
;     *(u32x4*)(KDT + d * 64 + cg * 16) = (u32x4){kd[0], kd[1], kd[2], kd[3]}; *(u32x4*)(KDT + d * 64 + cg * 16 + 8) = (u32x4){kd[4], kd[5], kd[6], kd[7]};
;     if (cg == 0) DEC[d] = eblast;
	ds_write_b16 v78, v63 offset:8192
	global_store_short v[66:67], v63, off
	v_add_f32_e32 v63, v133, v62
	v_mul_f32_e32 v63, 0x3fb8aa3b, v63
	v_exp_f32_e32 v63, v63
	v_lshlrev_b32_e32 v65, 16, v113
	v_mul_f32_e32 v65, 0x3db504f3, v65
	v_lshl_add_u64 v[100:101], s[66:67], 0, v[44:45]
	v_rcp_f32_e32 v66, v63
	v_mul_f32_e32 v63, v65, v63
	v_bfe_u32 v65, v63, 16, 1
	v_add3_u32 v63, v63, v65, s55
	v_add_f32_e32 v65, v134, v62
	v_lshrrev_b32_e32 v63, 16, v63
	v_mul_f32_e32 v65, 0x3fb8aa3b, v65
	global_store_short v[100:101], v63, off
	v_exp_f32_e32 v100, v65
	v_lshlrev_b32_e32 v67, 16, v108
	v_mul_f32_e32 v67, 0x3db504f3, v67
	v_mul_f32_e32 v67, v67, v100
	v_rcp_f32_e32 v65, v100
	v_bfe_u32 v100, v67, 16, 1
	v_add3_u32 v67, v67, v100, s55
	v_lshrrev_b32_e32 v102, 16, v67
	v_add_f32_e32 v67, v135, v62
	v_lshl_add_u64 v[100:101], s[66:67], 0, v[46:47]
	v_mul_f32_e32 v67, 0x3fb8aa3b, v67
	global_store_short v[100:101], v102, off
	v_exp_f32_e32 v101, v67
	v_lshlrev_b32_e32 v100, 16, v106
	v_mul_f32_e32 v100, 0x3db504f3, v100
	v_mul_f32_e32 v100, v100, v101
	v_rcp_f32_e32 v67, v101
	v_bfe_u32 v101, v100, 16, 1
	v_add3_u32 v100, v100, v101, s55
	v_lshrrev_b32_e32 v104, 16, v100
	v_lshl_add_u64 v[100:101], s[66:67], 0, v[48:49]
	global_store_short v[100:101], v104, off
	v_lshlrev_b32_e32 v101, 16, v103
	v_lshlrev_b32_e32 v100, 16, v99
	v_pk_mul_f32 v[64:65], v[64:65], v[100:101]
	v_lshl_add_u64 v[100:101], s[66:67], 0, v[52:53]
	v_bfe_u32 v99, v64, 16, 1
	v_add3_u32 v99, v64, v99, s55
	ds_write_b16_d16_hi v78, v99 offset:25600
	ds_write_b16 v79, v63 offset:8192
	v_lshlrev_b32_e32 v99, 16, v98
	v_lshlrev_b32_e32 v98, 16, v97
	v_pk_mul_f32 v[66:67], v[66:67], v[98:99]
	v_pk_mul_f32 v[98:99], v[2:3], v[64:65] op_sel_hi:[0,1]
	v_bfe_u32 v63, v66, 16, 1
	v_add3_u32 v63, v66, v63, s55
	ds_write_b16_d16_hi v79, v63 offset:25600
	v_bfe_u32 v63, v65, 16, 1
	v_add3_u32 v63, v65, v63, s55
	ds_write_b16_d16_hi v80, v63 offset:25600
	v_bfe_u32 v63, v67, 16, 1
	v_add3_u32 v63, v67, v63, s55
	ds_write_b16 v80, v102 offset:8192
	ds_write_b16_d16_hi v81, v63 offset:25600
	v_add_f32_e32 v63, v136, v62
	v_mul_f32_e32 v63, 0x3fb8aa3b, v63
	v_exp_f32_e32 v63, v63
	v_pk_mul_f32 v[64:65], v[2:3], v[66:67] op_sel_hi:[0,1]
	v_lshlrev_b32_e32 v66, 16, v96
	v_mul_f32_e32 v67, 0x3db504f3, v66
	v_rcp_f32_e32 v66, v63
	v_mul_f32_e32 v63, v67, v63
	v_bfe_u32 v67, v63, 16, 1
	v_add3_u32 v63, v63, v67, s55
	v_lshrrev_b32_e32 v63, 16, v63
	v_lshl_add_u64 v[96:97], s[66:67], 0, v[50:51]
	ds_write_b16 v81, v104 offset:8192
	ds_write_b16 v82, v63 offset:8192
	global_store_short v[96:97], v63, off
	v_add_f32_e32 v63, v137, v62
	v_mul_f32_e32 v63, 0x3fb8aa3b, v63
	v_exp_f32_e32 v63, v63
	v_lshlrev_b32_e32 v67, 16, v95
	v_mul_f32_e32 v67, 0x3db504f3, v67
	v_add_f32_e32 v3, v62, v3
	v_rcp_f32_e32 v96, v63
	v_mul_f32_e32 v63, v67, v63
	v_bfe_u32 v67, v63, 16, 1
	v_add3_u32 v63, v63, v67, s55
	v_lshrrev_b32_e32 v102, 16, v63
	v_add_f32_e32 v63, v138, v62
	v_mul_f32_e32 v63, 0x3fb8aa3b, v63
	v_mul_f32_e32 v3, 0x3fb8aa3b, v3
	v_exp_f32_e32 v63, v63
	v_exp_f32_e32 v3, v3
	v_lshlrev_b32_e32 v67, 16, v94
	v_lshlrev_b32_e32 v62, 16, v93
	v_mul_f32_e32 v94, 0x3db504f3, v67
	v_mul_f32_e32 v62, 0x3db504f3, v62
	v_rcp_f32_e32 v67, v63
	v_mul_f32_e32 v63, v94, v63
	v_rcp_f32_e32 v97, v3
	v_mul_f32_e32 v3, v62, v3
	v_bfe_u32 v94, v63, 16, 1
	v_bfe_u32 v62, v3, 16, 1
	v_add3_u32 v63, v63, v94, s55
	v_add3_u32 v3, v3, v62, s55
	global_store_short v[100:101], v102, off
	v_lshrrev_b32_e32 v100, 16, v63
	v_lshl_add_u64 v[94:95], s[66:67], 0, v[54:55]
	v_lshrrev_b32_e32 v3, 16, v3
	v_lshl_add_u64 v[62:63], s[66:67], 0, v[56:57]
	global_store_short v[94:95], v100, off
	global_store_short v[62:63], v3, off
	v_lshlrev_b32_e32 v63, 16, v92
	v_lshlrev_b32_e32 v62, 16, v91
	v_pk_mul_f32 v[62:63], v[66:67], v[62:63]
	v_lshlrev_b32_e32 v67, 16, v90
	v_bfe_u32 v66, v62, 16, 1
	v_add3_u32 v66, v62, v66, s55
	ds_write_b16_d16_hi v82, v66 offset:25600
	ds_write_b16 v83, v102 offset:8192
	v_lshlrev_b32_e32 v66, 16, v89
	v_pk_mul_f32 v[66:67], v[96:97], v[66:67]
	v_pk_mul_f32 v[90:91], v[2:3], v[62:63] op_sel_hi:[0,1]
	v_bfe_u32 v89, v66, 16, 1
	v_bfe_u32 v62, v63, 16, 1
	v_add3_u32 v89, v66, v89, s55
	v_add3_u32 v62, v63, v62, s55
	ds_write_b16_d16_hi v83, v89 offset:25600
	ds_write_b16 v84, v100 offset:8192
	ds_write_b16_d16_hi v84, v62 offset:25600
	v_pk_mul_f32 v[62:63], v[2:3], v[66:67] op_sel_hi:[0,1]
	ds_write_b16 v85, v3 offset:8192
	v_bfe_u32 v3, v67, 16, 1
	v_add3_u32 v3, v67, v3, s55
	v_bfe_u32 v67, v7, 16, 1
	v_bfe_u32 v66, v60, 16, 1
	v_bfe_u32 v89, v6, 16, 1
	v_add3_u32 v67, v7, v67, s55
	v_bfe_u32 v7, v58, 16, 1
	ds_write_b16_d16_hi v85, v3 offset:25600
	v_bfe_u32 v3, v61, 16, 1
	v_add3_u32 v89, v6, v89, s55
	v_add3_u32 v6, v60, v66, s55
	v_bfe_u32 v60, v59, 16, 1
	v_add3_u32 v7, v58, v7, s55
	v_add3_u32 v3, v61, v3, s55
	v_bfe_u32 v61, v4, 16, 1
	v_bfe_u32 v66, v5, 16, 1
	v_add3_u32 v59, v59, v60, s55
	v_lshrrev_b32_e32 v58, 16, v7
	v_add3_u32 v5, v5, v66, s55
	v_add3_u32 v4, v4, v61, s55
	v_lshrrev_b32_e32 v7, 16, v59
	v_and_or_b32 v6, v6, s45, v58
	v_lshl_add_u64 v[58:59], s[66:67], 0, v[24:25]
	v_lshrrev_b32_e32 v4, 16, v4
	v_lshrrev_b32_e32 v5, 16, v5
	v_add_co_u32_e32 v58, vcc, s56, v58
	v_and_or_b32 v7, v3, s45, v7
	v_and_or_b32 v5, v67, s45, v5
	v_and_or_b32 v4, v89, s45, v4
	v_addc_co_u32_e32 v59, vcc, 0, v59, vcc
	global_store_dwordx4 v[58:59], v[4:7], off
	v_bfe_u32 v61, v90, 16, 1
	v_bfe_u32 v3, v63, 16, 1
	v_bfe_u32 v4, v62, 16, 1
	v_bfe_u32 v6, v64, 16, 1
	v_add3_u32 v60, v64, v6, s55
	v_add3_u32 v4, v62, v4, s55
	v_bfe_u32 v6, v98, 16, 1
	v_bfe_u32 v7, v99, 16, 1
	v_bfe_u32 v62, v91, 16, 1
	v_bfe_u32 v5, v65, 16, 1
	v_add3_u32 v62, v91, v62, s55
	v_add3_u32 v61, v90, v61, s55
	v_add3_u32 v7, v99, v7, s55
	v_add3_u32 v6, v98, v6, s55
	v_add3_u32 v5, v65, v5, s55
	v_add3_u32 v3, v63, v3, s55
	v_lshrrev_b32_e32 v63, 16, v6
	v_lshrrev_b32_e32 v64, 16, v7
	v_lshrrev_b32_e32 v6, 16, v61
	v_lshrrev_b32_e32 v7, 16, v62
	v_and_or_b32 v7, v3, s45, v7
	v_and_or_b32 v6, v4, s45, v6
	v_and_or_b32 v5, v5, s45, v64
	v_and_or_b32 v4, v60, s45, v63
	global_store_dwordx4 v[58:59], v[4:7], off offset:16
	s_and_saveexec_b64 s[0:1], s[4:5]
	s_cbranch_execz .LBB0_266
	v_readlane_b32 s60, v254, 25
	v_readlane_b32 s66, v254, 31
	v_readlane_b32 s67, v254, 32
	v_readlane_b32 s61, v254, 26
	v_readlane_b32 s62, v254, 27
	v_lshl_add_u64 v[4:5], s[66:67], 0, v[18:19]
	v_readlane_b32 s63, v254, 28
	v_readlane_b32 s64, v254, 29
	v_readlane_b32 s65, v254, 30
	global_store_dword v[4:5], v2, off
